# baseline (speedup 1.0000x reference)
_Z11knrm_kernelPKfS0_PKiS2_S0_Pf:
	s_load_dwordx8 s[4:11], s[0:1], 0x0
	s_load_dwordx4 s[12:15], s[0:1], 0x20
	v_lshrrev_b32_e32 v1, 6, v0
	v_and_b32_e32 v120, 63, v0
	v_lshrrev_b32_e32 v100, 4, v0
	v_and_b32_e32 v123, 15, v0
	v_lshlrev_b32_e32 v124, 5, v1
	s_lshl_b32 s3, s2, 5
	v_lshl_or_b32 v8, s2, 8, v124
	v_or_b32_e32 v2, s3, v100
	s_movk_i32 s3, 0x4b0
	v_mul_lo_u32 v2, v2, s3
	v_mul_lo_u32 v99, v8, s3
	v_lshlrev_b32_e32 v132, 4, v120
	v_min_u32_e32 v193, 23, v120
	v_lshl_add_u32 v3, v123, 4, v2
	v_min_u32_e32 v4, 10, v123
	v_add_u32_e32 v192, v99, v132
	v_lshlrev_b32_e32 v193, 4, v193
	s_movk_i32 s27, 0x1000
	s_movk_i32 s28, 0x2000
	v_lshl_add_u32 v2, v4, 4, v2
	v_add3_u32 v193, v99, v193, s28
	s_mov_b32 s19, 0x20000
	s_mov_b32 s18, 0x4b00000
	s_waitcnt lgkmcnt(0)
	s_mov_b64 s[16:17], s[6:7]
	s_and_b32 s5, s5, 0xffff
	s_mov_b32 s6, 0x960000
	s_mov_b32 s7, s19
	s_and_b32 s17, s17, 0xffff
	buffer_load_dwordx4 v[90:93], v3, s[4:7], 0 offen nt
	buffer_load_dwordx4 v[86:89], v3, s[4:7], 0 offen offset:256 nt
	buffer_load_dwordx4 v[82:85], v3, s[4:7], 0 offen offset:512 nt
	buffer_load_dwordx4 v[78:81], v3, s[4:7], 0 offen offset:768 nt
	buffer_load_dwordx4 v[94:97], v2, s[4:7], 0 offen offset:1024 nt
	buffer_load_dwordx4 v[2:5], v192, s[16:19], 0 offen nt
	buffer_load_dwordx4 v[14:17], v192, s[16:19], 0 offen offset:1024 nt
	buffer_load_dwordx4 v[34:37], v192, s[16:19], 0 offen offset:2048 nt
	buffer_load_dwordx4 v[46:49], v192, s[16:19], 0 offen offset:3072 nt
	buffer_load_dwordx4 v[54:57], v192, s[16:19], s27 offen nt
	buffer_load_dwordx4 v[58:61], v192, s[16:19], s27 offen offset:1024 nt
	buffer_load_dwordx4 v[62:65], v192, s[16:19], s27 offen offset:2048 nt
	buffer_load_dwordx4 v[66:69], v192, s[16:19], s27 offen offset:3072 nt
	buffer_load_dwordx4 v[70:73], v192, s[16:19], s28 offen nt
	buffer_load_dwordx4 v[74:77], v193, s[16:19], 0 offen offset:1024 nt
	v_lshlrev_b32_e32 v42, 2, v0
	v_bfe_u32 v43, v0, 2, 2
	v_and_or_b32 v98, v42, 12, v43
	v_and_or_b32 v6, v98, 7, v8
	v_ashrrev_i32_e32 v7, 31, v6
	s_movk_i32 s0, 0x160
	v_lshl_add_u64 v[6:7], v[6:7], 2, s[10:11]
	v_lshrrev_b32_e32 v121, 5, v0
	v_cmp_gt_u32_e64 s[0:1], s0, v0
	s_nop 1
	v_cndmask_b32_e64 v44, 10, v121, s[0:1]
	v_lshlrev_b32_e32 v44, 2, v44
	s_lshl_b32 s3, s2, 5
	v_and_b32_e32 v122, 31, v0
	v_or_b32_e32 v42, s3, v122
	v_ashrrev_i32_e32 v43, 31, v42
	v_lshl_add_u64 v[42:43], v[42:43], 2, s[8:9]
	s_mov_b32 s3, 0
	v_mul_u32_u24_e32 v131, 0x2600, v1
	v_cmp_gt_u32_e64 s[4:5], 16, v120
	s_and_saveexec_b64 s[6:7], s[4:5]
	s_movk_i32 s8, 0x260
	v_mov_b32_e32 v102, 0
	v_mad_u32_u24 v101, v120, s8, v131
	v_mov_b32_e32 v103, v102
	ds_write_b64 v101, v[102:103] offset:20056
	s_or_b64 exec, exec, s[6:7]
	v_cmp_lt_u32_e32 vcc, 10, v123
	s_waitcnt vmcnt(13)
	v_mul_f32_e32 v101, v87, v87
	v_mov_b32_e32 v106, v92
	s_waitcnt vmcnt(10)
	v_cndmask_b32_e64 v103, v97, 0, vcc
	v_cndmask_b32_e64 v102, v96, 0, vcc
	v_mov_b32_e32 v96, v91
	v_mov_b32_e32 v97, v83
	v_cndmask_b32_e64 v105, v95, 0, vcc
	v_cndmask_b32_e64 v104, v94, 0, vcc
	v_mov_b32_e32 v94, v90
	v_mov_b32_e32 v95, v82
	v_pk_mul_f32 v[96:97], v[96:97], v[96:97]
	v_mov_b32_e32 v107, v84
	v_fmac_f32_e32 v101, v86, v86
	v_pk_fma_f32 v[94:95], v[94:95], v[94:95], v[96:97]
	v_mov_b32_e32 v108, v93
	v_mov_b32_e32 v109, v85
	v_fmac_f32_e32 v101, v88, v88
	v_pk_fma_f32 v[94:95], v[106:107], v[106:107], v[94:95]
	v_fmac_f32_e32 v101, v89, v89
	v_pk_fma_f32 v[94:95], v[108:109], v[108:109], v[94:95]
	v_mov_b32_e32 v96, v79
	v_add_f32_e32 v94, v94, v101
	v_mov_b32_e32 v97, v105
	v_add_f32_e32 v101, v94, v95
	v_mov_b32_e32 v94, v78
	v_mov_b32_e32 v95, v104
	v_pk_mul_f32 v[96:97], v[96:97], v[96:97]
	s_mov_b32 s21, 0xf800000
	v_pk_fma_f32 v[94:95], v[94:95], v[94:95], v[96:97]
	v_mov_b32_e32 v96, v80
	v_mov_b32_e32 v97, v102
	v_pk_fma_f32 v[94:95], v[96:97], v[96:97], v[94:95]
	v_mov_b32_e32 v96, v81
	v_mov_b32_e32 v97, v103
	v_pk_fma_f32 v[94:95], v[96:97], v[96:97], v[94:95]
	v_mov_b32_e32 v135, 0x260
	v_add_f32_e32 v94, v101, v94
	v_add_f32_e32 v94, v94, v95
	v_mbcnt_lo_u32_b32 v95, -1, 0
	v_mbcnt_hi_u32_b32 v95, -1, v95
	v_and_b32_e32 v97, 64, v95
	v_add_u32_e32 v101, 64, v97
	s_movk_i32 s8, 0x260
	v_add_u32_e32 v137, 0x4b00, v99
	s_movk_i32 s10, 0x1b5
	v_mov_b32_e32 v99, 0x36a00
	v_mov_b32_e32 v111, 0x666c0
	v_mov_b32_e32 v113, 0x6d400
	v_mov_b32_e32 v115, 0x74140
	s_mov_b32 s20, 0xbeb17218
	s_mov_b32 s22, 0x44132d1f
	v_mov_b32_e32 v161, 0xc47a0000
	v_add_f32_dpp v96, v94, v94 quad_perm:[1,0,3,2] row_mask:0xf bank_mask:0xf
	s_nop 1
	v_add_f32_dpp v94, v96, v96 quad_perm:[2,3,0,1] row_mask:0xf bank_mask:0xf
	s_nop 1
	v_add_f32_dpp v96, v94, v94 row_half_mirror row_mask:0xf bank_mask:0xf
	s_nop 1
	v_add_f32_dpp v94, v96, v96 row_mirror row_mask:0xf bank_mask:0xf
	v_mul_f32_e32 v96, 0x4f800000, v94
	v_cmp_gt_f32_e32 vcc, s21, v94
	s_nop 1
	v_cndmask_b32_e32 v94, v94, v96, vcc
	v_sqrt_f32_e32 v96, v94
	s_nop 0
	v_add_u32_e32 v106, -1, v96
	v_fma_f32 v107, -v106, v96, v94
	v_cmp_ge_f32_e64 s[6:7], 0, v107
	v_add_u32_e32 v107, 1, v96
	s_nop 0
	v_cndmask_b32_e64 v106, v96, v106, s[6:7]
	v_fma_f32 v96, -v107, v96, v94
	v_cmp_lt_f32_e64 s[6:7], 0, v96
	s_nop 1
	v_cndmask_b32_e64 v96, v106, v107, s[6:7]
	v_mul_f32_e32 v106, 0x37800000, v96
	v_cndmask_b32_e32 v96, v96, v106, vcc
	v_cmp_class_f32_e32 vcc, v94, v135
	s_nop 1
	v_cndmask_b32_e32 v94, v96, v94, vcc
	v_add_f32_e32 v96, 0x29e12e13, v94
	v_div_scale_f32 v106, s[6:7], v96, v96, 1.0
	v_rcp_f32_e32 v107, v106
	v_mov_b32_e32 v94, 0
	v_cmp_gt_u32_e64 s[6:7], 48, v120
	v_mov_b32_e32 v116, v94
	v_fma_f32 v108, -v106, v107, 1.0
	v_fmac_f32_e32 v107, v108, v107
	v_div_scale_f32 v108, vcc, 1.0, v96, 1.0
	v_mul_f32_e32 v109, v108, v107
	v_fma_f32 v110, -v106, v109, v108
	v_fmac_f32_e32 v109, v110, v107
	v_fma_f32 v106, -v106, v109, v108
	v_div_fmas_f32 v106, v106, v107, v109
	v_div_fixup_f32 v96, v106, v96, 1.0
	v_lshlrev_b32_e32 v106, 3, v123
	v_pk_mul_f32 v[82:83], v[96:97], v[82:83] op_sel_hi:[0,1]
	v_pk_mul_f32 v[84:85], v[96:97], v[84:85] op_sel_hi:[0,1]
	v_pk_mul_f32 v[78:79], v[96:97], v[78:79] op_sel_hi:[0,1]
	v_pk_mul_f32 v[80:81], v[96:97], v[80:81] op_sel_hi:[0,1]
	v_mad_u32_u24 v100, v100, s8, v106
	v_cvt_pk_f16_f32 v82, v82, v83
	v_cvt_pk_f16_f32 v83, v84, v85
	v_cvt_pk_f16_f32 v78, v78, v79
	v_cvt_pk_f16_f32 v79, v80, v81
	ds_write2_b64 v100, v[82:83], v[78:79] offset0:32 offset1:48
	v_min_u32_e32 v82, 23, v120
	v_mov_b32_e32 v83, 0x2400
	v_lshl_or_b32 v138, v82, 4, v83
	v_xor_b32_e32 v83, 16, v95
	v_cmp_lt_i32_e32 vcc, v83, v101
	v_pk_mul_f32 v[90:91], v[96:97], v[90:91] op_sel_hi:[0,1]
	v_pk_mul_f32 v[92:93], v[96:97], v[92:93] op_sel_hi:[0,1]
	v_cndmask_b32_e32 v83, v95, v83, vcc
	v_lshlrev_b32_e32 v133, 2, v83
	v_xor_b32_e32 v83, 32, v95
	v_pk_mul_f32 v[86:87], v[96:97], v[86:87] op_sel_hi:[0,1]
	v_pk_mul_f32 v[88:89], v[96:97], v[88:89] op_sel_hi:[0,1]
	v_pk_mul_f32 v[78:79], v[96:97], v[104:105] op_sel_hi:[0,1]
	v_pk_mul_f32 v[80:81], v[96:97], v[102:103] op_sel_hi:[0,1]
	v_cmp_lt_i32_e32 vcc, v83, v101
	v_cvt_pk_f16_f32 v90, v90, v91
	v_cvt_pk_f16_f32 v91, v92, v93
	v_cvt_pk_f16_f32 v86, v86, v87
	v_cvt_pk_f16_f32 v87, v88, v89
	v_cvt_pk_f16_f32 v78, v78, v79
	v_cvt_pk_f16_f32 v79, v80, v81
	v_mov_b32_e32 v81, 0x17c00
	v_cndmask_b32_e32 v83, v95, v83, vcc
	ds_write2_b64 v100, v[90:91], v[86:87] offset1:16
	v_sub_u32_e64 v80, v123, 11 clamp
	v_lshl_or_b32 v81, v1, 7, v81
	v_lshlrev_b32_e32 v134, 2, v83
	v_or_b32_e32 v83, 64, v120
	v_mov_b32_e32 v86, 0x6d40
	v_mov_b32_e32 v87, 0xda80
	v_mov_b32_e32 v89, 0x147c0
	v_mov_b32_e32 v91, 0x1b500
	v_mov_b32_e32 v93, 0x28f80
	v_mov_b32_e32 v96, 0x2fcc0
	v_mov_b32_e32 v101, 0x3d740
	v_mov_b32_e32 v103, 0x44480
	v_mov_b32_e32 v105, 0x4b1c0
	v_mov_b32_e32 v107, 0x58c40
	v_or_b32_e32 v109, 0x3c0, v0
	v_mad_i32_i24 v80, v80, -8, v100
	v_lshrrev_b32_e32 v82, 1, v120
	v_lshl_add_u32 v139, v120, 2, v81
	v_and_or_b32 v140, v120, 48, v81
	v_lshlrev_b32_e32 v81, 3, v120
	v_mul_u32_u24_e32 v84, 0x1b5, v83
	v_lshl_add_u32 v85, v83, 3, v131
	v_mad_u32_u24 v86, v83, s10, v86
	v_mad_u32_u24 v87, v83, s10, v87
	v_mad_u32_u24 v89, v83, s10, v89
	v_mad_u32_u24 v91, v83, s10, v91
	v_mad_u32_u24 v93, v83, s10, v93
	v_mad_u32_u24 v96, v83, s10, v96
	v_mad_u32_u24 v99, v83, s10, v99
	v_mad_u32_u24 v101, v83, s10, v101
	v_mad_u32_u24 v103, v83, s10, v103
	v_mad_u32_u24 v105, v83, s10, v105
	v_mad_u32_u24 v107, v83, s10, v107
	v_mul_u32_u24_e32 v110, 0x1b5, v109
	v_mad_u32_u24 v111, v83, s10, v111
	v_mad_u32_u24 v113, v83, s10, v113
	v_mad_u32_u24 v83, v83, s10, v115
	ds_write_b64 v80, v[78:79] offset:512
	v_mul_u32_u24_e32 v78, 0x260, v123
	v_and_b32_e32 v82, 24, v82
	v_lshrrev_b32_e32 v84, 12, v84
	v_add_u32_e32 v141, v131, v81
	v_lshrrev_b32_e32 v86, 12, v86
	v_lshrrev_b32_e32 v87, 12, v87
	v_lshrrev_b32_e32 v89, 12, v89
	v_lshrrev_b32_e32 v91, 12, v91
	v_lshrrev_b32_e32 v93, 12, v93
	v_lshrrev_b32_e32 v96, 12, v96
	v_lshrrev_b32_e32 v99, 12, v99
	v_lshrrev_b32_e32 v101, 12, v101
	v_lshrrev_b32_e32 v103, 12, v103
	v_lshrrev_b32_e32 v105, 12, v105
	v_lshrrev_b32_e32 v107, 12, v107
	v_lshrrev_b32_e32 v110, 12, v110
	v_lshrrev_b32_e32 v111, 12, v111
	v_lshrrev_b32_e32 v113, 12, v113
	v_lshrrev_b32_e32 v83, 12, v83
	v_and_b32_e32 v79, 48, v0
	v_mad_u32_u24 v80, v98, s8, v131
	v_and_b32_e32 v84, 8, v84
	v_add_u32_e32 v81, 0x400, v141
	v_and_b32_e32 v86, 24, v86
	v_add_u32_e32 v88, 0x600, v141
	v_and_b32_e32 v87, 24, v87
	v_add_u32_e32 v90, 0x800, v141
	v_and_b32_e32 v89, 56, v89
	v_add_u32_e32 v92, 0xa00, v141
	v_and_b32_e32 v91, 56, v91
	v_add_u32_e32 v95, 0xe00, v141
	v_and_b32_e32 v93, 56, v93
	v_add_u32_e32 v98, 0x1000, v141
	v_and_b32_e32 v96, 56, v96
	v_add_u32_e32 v100, 0x1200, v141
	v_and_b32_e32 v99, 0x78, v99
	v_add_u32_e32 v102, 0x1400, v141
	v_and_b32_e32 v101, 0x78, v101
	v_add_u32_e32 v104, 0x1600, v141
	v_and_b32_e32 v103, 0x58, v103
	v_add_u32_e32 v106, 0x1800, v141
	v_and_b32_e32 v105, 0x58, v105
	v_add_u32_e32 v108, 0x1c00, v141
	v_and_b32_e32 v107, 0x78, v107
	v_lshl_add_u32 v109, v109, 3, v131
	v_and_b32_e32 v110, 0x78, v110
	v_add_u32_e32 v112, 0x2000, v141
	v_and_b32_e32 v111, 0x78, v111
	v_add_u32_e32 v114, 0x2200, v141
	v_and_b32_e32 v113, 0x78, v113
	v_add_u32_e32 v115, 0x2400, v141
	v_and_b32_e32 v83, 0xf8, v83
	s_movk_i32 s10, 0x4c00
	v_add_u32_e32 v78, v78, v82
	v_mad_u32_u24 v136, v123, s8, v79
	v_cmp_gt_u32_e64 s[8:9], 24, v120
	v_add3_u32 v142, v80, v79, s10
	v_add_u32_e32 v143, v85, v84
	v_add_u32_e32 v144, v81, v86
	v_add_u32_e32 v145, v88, v87
	v_add_u32_e32 v146, v90, v89
	v_add_u32_e32 v147, v92, v91
	v_add_u32_e32 v148, v95, v93
	v_add_u32_e32 v149, v98, v96
	v_add_u32_e32 v150, v100, v99
	v_add_u32_e32 v151, v102, v101
	v_add_u32_e32 v152, v104, v103
	v_add_u32_e32 v153, v106, v105
	v_add_u32_e32 v154, v108, v107
	v_add_u32_e32 v155, v109, v110
	v_add_u32_e32 v156, v112, v111
	v_add_u32_e32 v157, v114, v113
	v_add_u32_e32 v158, v115, v83
	v_add_u32_e32 v159, v80, v82
	v_add_u32_e32 v160, 64, v78
	v_mov_b32_e32 v96, 0xc604b4df
	v_mov_b32_e32 v95, v94
	v_mov_b32_e32 v98, v94
	v_mov_b32_e32 v99, v94
	v_mov_b32_e32 v100, v94
	v_mov_b32_e32 v101, v94
	v_mov_b32_e32 v102, v94
	v_mov_b32_e32 v103, v94
	v_mov_b32_e32 v104, v94
	v_mov_b32_e32 v105, v94
	v_mov_b32_e32 v106, v94
	v_mov_b32_e32 v107, v94
	v_mov_b32_e32 v108, v94
	v_mov_b32_e32 v109, v94
	v_mov_b32_e32 v110, v94
	v_mov_b32_e32 v111, v94
	v_mov_b32_e32 v112, v94
	v_mov_b32_e32 v113, v94
	v_mov_b32_e32 v114, v94
	v_mov_b32_e32 v115, v94
	v_mov_b32_e32 v117, v94
	s_waitcnt lgkmcnt(0)
	s_barrier
	global_load_dword v125, v[6:7], off
	global_load_dword v126, v[6:7], off offset:64
	global_load_dword v127, v[6:7], off offset:96
	global_load_dword v190, v[6:7], off offset:32
	global_load_dword v118, v44, s[12:13]
	global_load_dword v119, v[42:43], off
	s_mov_b32 s26, 0x2580
	s_mov_b32 s27, 0x3580
	s_mov_b32 s28, 0x4580
	buffer_load_dwordx4 v[6:9], v192, s[16:19], s26 offen nt
	buffer_load_dwordx4 v[10:13], v192, s[16:19], s26 offen offset:1024 nt
	buffer_load_dwordx4 v[18:21], v192, s[16:19], s26 offen offset:2048 nt
	buffer_load_dwordx4 v[22:25], v192, s[16:19], s26 offen offset:3072 nt
	buffer_load_dwordx4 v[26:29], v192, s[16:19], s27 offen nt
	buffer_load_dwordx4 v[30:33], v192, s[16:19], s27 offen offset:1024 nt
	buffer_load_dwordx4 v[38:41], v192, s[16:19], s27 offen offset:2048 nt
	buffer_load_dwordx4 v[42:45], v192, s[16:19], s27 offen offset:3072 nt
	buffer_load_dwordx4 v[50:53], v192, s[16:19], s28 offen nt
	buffer_load_dwordx4 v[186:189], v193, s[16:19], s26 offen offset:1024 nt
	s_waitcnt vmcnt(25)
	v_cvt_pk_f16_f32 v79, v4, v5
	v_cvt_pk_f16_f32 v78, v2, v3
	ds_write_b64 v141, v[78:79] offset:19456
	s_waitcnt vmcnt(24)
	v_cvt_pk_f16_f32 v79, v16, v17
	v_cvt_pk_f16_f32 v78, v14, v15
	ds_write_b64 v143, v[78:79] offset:19456
	s_waitcnt vmcnt(23)
	v_cvt_pk_f16_f32 v79, v36, v37
	v_cvt_pk_f16_f32 v78, v34, v35
	ds_write_b64 v144, v[78:79] offset:19456
	s_waitcnt vmcnt(22)
	v_cvt_pk_f16_f32 v79, v48, v49
	v_cvt_pk_f16_f32 v78, v46, v47
	ds_write_b64 v145, v[78:79] offset:19456
	s_waitcnt vmcnt(21)
	v_cvt_pk_f16_f32 v79, v56, v57
	v_cvt_pk_f16_f32 v78, v54, v55
	ds_write_b64 v146, v[78:79] offset:19456
	s_waitcnt vmcnt(20)
	v_cvt_pk_f16_f32 v79, v60, v61
	v_cvt_pk_f16_f32 v78, v58, v59
	ds_write_b64 v147, v[78:79] offset:19456
	s_waitcnt vmcnt(19)
	v_cvt_pk_f16_f32 v79, v64, v65
	v_cvt_pk_f16_f32 v78, v62, v63
	ds_write_b64 v141, v[78:79] offset:22568
	s_waitcnt vmcnt(18)
	v_cvt_pk_f16_f32 v79, v68, v69
	v_cvt_pk_f16_f32 v78, v66, v67
	ds_write_b64 v148, v[78:79] offset:19456
	s_waitcnt vmcnt(17)
	v_cvt_pk_f16_f32 v79, v72, v73
	v_cvt_pk_f16_f32 v78, v70, v71
	ds_write_b64 v149, v[78:79] offset:19456
	s_waitcnt vmcnt(16)
	v_cvt_pk_f16_f32 v79, v76, v77
	v_cvt_pk_f16_f32 v78, v74, v75
	s_and_saveexec_b64 s[12:13], s[8:9]
	ds_write_b64 v150, v[78:79] offset:19456
	s_or_b64 exec, exec, s[12:13]
	s_waitcnt vmcnt(10)
	v_cmp_lt_i32_e64 s[30:31], 1, v125
	v_cmp_lt_i32_e64 s[32:33], 1, v190
	v_cmp_lt_i32_e64 s[34:35], 1, v126
	v_cmp_lt_i32_e64 s[36:37], 1, v127
	v_cndmask_b32_e64 v191, 0, 1, s[30:31]
	v_cndmask_b32_e64 v190, 0, 2, s[32:33]
	v_cndmask_b32_e64 v126, 0, 4, s[34:35]
	v_cndmask_b32_e64 v127, 0, 8, s[36:37]
	v_or3_b32 v191, v191, v190, v126
	v_or_b32_e32 v191, v191, v127
	s_mov_b32 s26, 0x4b00
	s_mov_b32 s27, 0x5b00
	s_mov_b32 s28, 0x6b00
	buffer_load_dwordx4 v[2:5], v192, s[16:19], s26 offen nt
	buffer_load_dwordx4 v[14:17], v192, s[16:19], s26 offen offset:1024 nt
	buffer_load_dwordx4 v[34:37], v192, s[16:19], s26 offen offset:2048 nt
	buffer_load_dwordx4 v[46:49], v192, s[16:19], s26 offen offset:3072 nt
	buffer_load_dwordx4 v[54:57], v192, s[16:19], s27 offen nt
	buffer_load_dwordx4 v[58:61], v192, s[16:19], s27 offen offset:1024 nt
	buffer_load_dwordx4 v[62:65], v192, s[16:19], s27 offen offset:2048 nt
	buffer_load_dwordx4 v[66:69], v192, s[16:19], s27 offen offset:3072 nt
	buffer_load_dwordx4 v[70:73], v192, s[16:19], s28 offen nt
	buffer_load_dwordx4 v[74:77], v193, s[16:19], s26 offen offset:1024 nt
	s_mov_b32 s3, 0
	s_branch .LBB0_7
